# speedup vs baseline: 1.0108x; 1.0108x over previous
_Z8k2_fusedPKDF16_PKDv8_DF16_PKfS5_S5_PfPiS6_:
	v_readfirstlane_b32 s38, v0
	s_lshl_b32 s3, s2, 2
	s_ashr_i32 s16, s2, 4
	s_and_b32 s12, s3, 48
	s_lshl_b32 s2, s2, 4
	s_and_b32 s13, s2, 48
	s_add_i32 s2, s12, -2
	v_mul_u32_u24_e32 v1, 0x334, v0
	s_movk_i32 s15, 0xffec
	s_add_i32 s3, s13, -2
	v_lshrrev_b32_e32 v84, 2, v0
	v_mul_i32_i24_sdwa v2, v1, s15 dst_sel:DWORD dst_unused:UNUSED_PAD src0_sel:WORD_1 src1_sel:DWORD
	v_add_u32_sdwa v48, s2, v1 dst_sel:DWORD dst_unused:UNUSED_PAD src0_sel:DWORD src1_sel:WORD_1
	s_load_dwordx8 s[4:11], s[0:1], 0x0
	s_load_dwordx4 s[32:35], s[0:1], 0x20
	s_load_dwordx2 s[36:37], s[0:1], 0x38
	v_add3_u32 v49, s3, v84, v2
	v_max_i32_e32 v1, 0, v48
	s_lshl_b32 s14, s16, 12
	v_med3_i32 v2, v49, 0, 63
	v_lshlrev_b32_e32 v1, 6, v1
	v_or3_b32 v1, v1, v2, s14
	v_lshlrev_b32_e32 v2, 5, v1
	v_ashrrev_i32_e32 v3, 31, v2
	v_lshlrev_b32_e32 v85, 4, v0
	s_waitcnt lgkmcnt(0)
	v_lshl_add_u64 v[2:3], v[2:3], 1, s[4:5]
	v_and_b32_e32 v46, 48, v85
	v_mov_b32_e32 v47, 0
	v_or_b32_e32 v54, 0x200, v0
	v_lshl_add_u64 v[2:3], v[2:3], 0, v[46:47]
	v_mul_u32_u24_e32 v1, 0x334, v54
	global_load_dwordx4 v[18:21], v[2:3], off
	v_lshrrev_b32_e32 v86, 2, v54
	v_mul_i32_i24_sdwa v2, v1, s15 dst_sel:DWORD dst_unused:UNUSED_PAD src0_sel:WORD_1 src1_sel:DWORD
	v_add_u32_sdwa v50, s2, v1 dst_sel:DWORD dst_unused:UNUSED_PAD src0_sel:DWORD src1_sel:WORD_1
	v_add3_u32 v51, s3, v86, v2
	v_min_u32_e32 v1, 63, v50
	v_med3_i32 v2, v51, 0, 63
	v_lshlrev_b32_e32 v1, 6, v1
	v_or3_b32 v1, v1, v2, s14
	v_lshlrev_b32_e32 v2, 5, v1
	v_or_b32_e32 v58, 0x400, v0
	v_ashrrev_i32_e32 v3, 31, v2
	v_lshlrev_b32_e32 v87, 4, v54
	v_mul_u32_u24_e32 v1, 0x667, v58
	v_lshl_add_u64 v[2:3], v[2:3], 1, s[4:5]
	v_and_b32_e32 v4, 48, v87
	v_mov_b32_e32 v5, v47
	v_lshrrev_b32_e32 v1, 17, v1
	v_lshl_add_u64 v[2:3], v[2:3], 0, v[4:5]
	v_mul_i32_i24_e32 v4, 0xffffffec, v1
	v_add_u32_e32 v52, s2, v1
	v_lshrrev_b32_e32 v88, 2, v58
	v_add3_u32 v53, s3, v88, v4
	v_min_u32_e32 v1, 63, v52
	v_med3_i32 v4, v53, 0, 63
	v_lshlrev_b32_e32 v1, 6, v1
	v_or3_b32 v1, v1, v4, s14
	v_lshlrev_b32_e32 v4, 5, v1
	v_ashrrev_i32_e32 v5, 31, v4
	v_or_b32_e32 v89, 0x600, v0
	v_lshl_add_u64 v[4:5], v[4:5], 1, s[4:5]
	v_min_u32_e32 v1, 0x63f, v89
	v_lshl_add_u64 v[4:5], v[4:5], 0, v[46:47]
	global_load_dwordx4 v[22:25], v[2:3], off
	global_load_dwordx4 v[26:29], v[4:5], off
	v_lshrrev_b32_e32 v2, 2, v1
	v_add_u32_e32 v2, s3, v2
	s_add_i32 s15, s12, 17
	v_add_u32_e32 v55, 0xfffffe84, v2
	s_min_u32 s2, s15, 63
	v_min_u32_e32 v2, 63, v55
	v_lshl_or_b32 v2, s2, 6, v2
	v_or_b32_e32 v2, s14, v2
	v_lshlrev_b32_e32 v2, 5, v2
	v_ashrrev_i32_e32 v3, 31, v2
	v_lshlrev_b32_e32 v1, 4, v1
	v_lshl_add_u64 v[2:3], v[2:3], 1, s[4:5]
	v_and_b32_e32 v4, 48, v1
	v_mov_b32_e32 v5, v47
	v_min_u32_e32 v1, 0x47f, v58
	v_lshrrev_b32_e32 v164, 1, v0
	v_lshl_add_u64 v[2:3], v[2:3], 0, v[4:5]
	v_lshlrev_b32_e32 v90, 4, v1
	v_and_b32_e32 v162, 16, v164
	global_load_dwordx4 v[30:33], v[2:3], off
	global_load_dwordx4 v[34:37], v85, s[6:7]
	global_load_dwordx4 v[38:41], v87, s[6:7]
	global_load_dwordx4 v[42:45], v90, s[6:7]
	s_nop 0
	global_load_dwordx4 v[2:5], v162, s[8:9]
	global_load_dwordx4 v[6:9], v162, s[8:9] offset:32
	global_load_dwordx4 v[10:13], v162, s[8:9] offset:64
	global_load_dwordx4 v[14:17], v162, s[8:9] offset:96
	v_or_b32_e32 v48, v48, v49
	v_cmp_gt_u32_e32 vcc, 64, v48
	v_or_b32_e32 v48, v50, v51
	v_cmp_gt_u32_e64 s[2:3], 64, v48
	v_or_b32_e32 v48, v52, v53
	v_and_b32_e32 v1, 63, v0
	v_and_b32_e32 v165, 31, v0
	v_cmp_gt_u32_e64 s[4:5], 64, v48
	v_or_b32_e32 v48, s15, v55
	v_lshrrev_b32_e32 v163, 6, v0
	v_cmp_gt_u32_e64 s[6:7], 64, v48
	s_movk_i32 s8, 0x50
	s_lshr_b32 s27, s12, 1
	s_lshr_b32 s26, s13, 1
	v_add_u32_e32 v48, s27, v163
	v_bfe_u32 v49, v0, 1, 3
	v_add_u32_e32 v49, s26, v49
	v_lshlrev_b32_e32 v48, 10, v48
	v_lshl_or_b32 v48, v49, 5, v48
	v_bfe_u32 v49, v0, 5, 1
	v_lshl_or_b32 v48, v49, 2, v48
	v_bfe_u32 v49, v0, 4, 1
	v_lshl_or_b32 v48, v49, 1, v48
	v_and_b32_e32 v49, 1, v0
	v_or_b32_e32 v48, v48, v49
	v_mul_u32_u24_e32 v210, 40, v48
	s_cmp_lt_u32 s38, 0xc0
	s_cbranch_scc0 .Lk2_late
	global_load_dwordx4 v[66:69], v210, s[10:11]
	global_load_dwordx4 v[50:53], v210, s[10:11] offset:16
	global_load_dwordx2 v[156:157], v210, s[10:11] offset:32
	global_load_dwordx4 v[70:73], v210, s[10:11] offset:320
	global_load_dwordx4 v[54:57], v210, s[10:11] offset:336
	global_load_dwordx2 v[154:155], v210, s[10:11] offset:352
	global_load_dwordx4 v[74:77], v210, s[10:11] offset:640
	global_load_dwordx4 v[58:61], v210, s[10:11] offset:656
	global_load_dwordx2 v[160:161], v210, s[10:11] offset:672
	global_load_dwordx4 v[78:81], v210, s[10:11] offset:960
	global_load_dwordx4 v[62:65], v210, s[10:11] offset:976
	global_load_dwordx2 v[158:159], v210, s[10:11] offset:992
	s_waitcnt vmcnt(22)
	v_cndmask_b32_e32 v19, 0, v19, vcc
	v_cndmask_b32_e32 v18, 0, v18, vcc
	v_cndmask_b32_e32 v21, 0, v21, vcc
	v_cndmask_b32_e32 v20, 0, v20, vcc
	v_mad_u32_u24 v47, v84, s8, v46
	ds_write_b128 v47, v[18:21]
	s_waitcnt vmcnt(21)
	v_cndmask_b32_e64 v19, 0, v23, s[2:3]
	v_cndmask_b32_e64 v18, 0, v22, s[2:3]
	v_cndmask_b32_e64 v21, 0, v25, s[2:3]
	v_cndmask_b32_e64 v20, 0, v24, s[2:3]
	v_mad_u32_u24 v22, v86, s8, v46
	ds_write_b128 v22, v[18:21]
	s_waitcnt vmcnt(20)
	v_cndmask_b32_e64 v19, 0, v27, s[4:5]
	v_cndmask_b32_e64 v18, 0, v26, s[4:5]
	v_cndmask_b32_e64 v21, 0, v29, s[4:5]
	v_cndmask_b32_e64 v20, 0, v28, s[4:5]
	v_mad_u32_u24 v22, v88, s8, v46
	ds_write_b128 v22, v[18:21]
	v_lshrrev_b32_e32 v22, 2, v89
	s_waitcnt vmcnt(19)
	v_cndmask_b32_e64 v19, 0, v31, s[6:7]
	v_cndmask_b32_e64 v18, 0, v30, s[6:7]
	v_cndmask_b32_e64 v21, 0, v33, s[6:7]
	v_cndmask_b32_e64 v20, 0, v32, s[6:7]
	v_mad_u32_u24 v22, v22, s8, v46
	ds_write_b128 v22, v[18:21]
	s_waitcnt vmcnt(18)
	ds_write_b128 v85, v[34:37] offset:57920
	s_waitcnt vmcnt(17)
	ds_write_b128 v87, v[38:41] offset:57920
	s_waitcnt vmcnt(16)
	ds_write_b128 v90, v[42:45] offset:57920
	s_branch .Lk2_stg_done
.Lk2_late:
	s_waitcnt vmcnt(10)
	v_cndmask_b32_e32 v19, 0, v19, vcc
	v_cndmask_b32_e32 v18, 0, v18, vcc
	v_cndmask_b32_e32 v21, 0, v21, vcc
	v_cndmask_b32_e32 v20, 0, v20, vcc
	v_mad_u32_u24 v47, v84, s8, v46
	ds_write_b128 v47, v[18:21]
	s_waitcnt vmcnt(9)
	v_cndmask_b32_e64 v19, 0, v23, s[2:3]
	v_cndmask_b32_e64 v18, 0, v22, s[2:3]
	v_cndmask_b32_e64 v21, 0, v25, s[2:3]
	v_cndmask_b32_e64 v20, 0, v24, s[2:3]
	v_mad_u32_u24 v22, v86, s8, v46
	ds_write_b128 v22, v[18:21]
	s_waitcnt vmcnt(8)
	v_cndmask_b32_e64 v19, 0, v27, s[4:5]
	v_cndmask_b32_e64 v18, 0, v26, s[4:5]
	v_cndmask_b32_e64 v21, 0, v29, s[4:5]
	v_cndmask_b32_e64 v20, 0, v28, s[4:5]
	v_mad_u32_u24 v22, v88, s8, v46
	ds_write_b128 v22, v[18:21]
	v_lshrrev_b32_e32 v22, 2, v89
	s_waitcnt vmcnt(7)
	v_cndmask_b32_e64 v19, 0, v31, s[6:7]
	v_cndmask_b32_e64 v18, 0, v30, s[6:7]
	v_cndmask_b32_e64 v21, 0, v33, s[6:7]
	v_cndmask_b32_e64 v20, 0, v32, s[6:7]
	v_mad_u32_u24 v22, v22, s8, v46
	ds_write_b128 v22, v[18:21]
	s_waitcnt vmcnt(6)
	ds_write_b128 v85, v[34:37] offset:57920
	s_waitcnt vmcnt(5)
	ds_write_b128 v87, v[38:41] offset:57920
	s_waitcnt vmcnt(4)
	ds_write_b128 v90, v[42:45] offset:57920
.Lk2_stg_done:
	v_lshlrev_b32_e32 v18, 4, v1
	s_waitcnt lgkmcnt(0)
	s_barrier
	s_cmp_lt_u32 s38, 0xc0
	s_cbranch_scc1 .Lk2_noload
	global_load_dwordx4 v[66:69], v210, s[10:11]
	global_load_dwordx4 v[50:53], v210, s[10:11] offset:16
	global_load_dwordx2 v[156:157], v210, s[10:11] offset:32
	global_load_dwordx4 v[70:73], v210, s[10:11] offset:320
	global_load_dwordx4 v[54:57], v210, s[10:11] offset:336
	global_load_dwordx2 v[154:155], v210, s[10:11] offset:352
	global_load_dwordx4 v[74:77], v210, s[10:11] offset:640
	global_load_dwordx4 v[58:61], v210, s[10:11] offset:656
	global_load_dwordx2 v[160:161], v210, s[10:11] offset:672
	global_load_dwordx4 v[78:81], v210, s[10:11] offset:960
	global_load_dwordx4 v[62:65], v210, s[10:11] offset:976
	global_load_dwordx2 v[158:159], v210, s[10:11] offset:992
.Lk2_noload:
	v_add_u32_e32 v19, 0xe240, v18
	ds_read_b128 v[150:153], v18 offset:57920
	ds_read_b128 v[146:149], v18 offset:58944
	ds_read_b128 v[142:145], v18 offset:59968
	ds_read_b128 v[138:141], v18 offset:60992
	ds_read_b128 v[134:137], v18 offset:62016
	ds_read_b128 v[130:133], v18 offset:63040
	ds_read_b128 v[126:129], v18 offset:64064
	ds_read_b128 v[122:125], v18 offset:65088
	ds_read_b128 v[118:121], v19 offset:8192
	ds_read_b128 v[114:117], v19 offset:9216
	ds_read_b128 v[110:113], v19 offset:10240
	ds_read_b128 v[106:109], v19 offset:11264
	ds_read_b128 v[102:105], v19 offset:12288
	ds_read_b128 v[98:101], v19 offset:13312
	ds_read_b128 v[94:97], v19 offset:14336
	ds_read_b128 v[90:93], v19 offset:15360
	ds_read_b128 v[86:89], v19 offset:16384
	ds_read_b128 v[82:85], v19 offset:17408
	v_lshl_or_b32 v166, v163, 5, v165
	v_mul_u32_u24_e32 v18, 0xe39, v166
	v_lshrrev_b32_e32 v168, 16, v18
	s_movk_i32 s4, 0xffee
	v_mad_i32_i24 v169, v168, s4, v166
	v_min_u32_e32 v19, 0x43, v166
	v_mad_u32_u24 v18, v168, 20, v169
	v_or_b32_e32 v165, 0x100, v19
	s_movk_i32 s2, 0xc0
	v_mul_lo_u32 v18, v18, s8
	v_mul_u32_u24_e32 v19, 0xe39, v165
	v_cmp_gt_u32_e32 vcc, s2, v0
	s_movk_i32 s2, 0xbf
	v_lshrrev_b32_e32 v167, 16, v19
	v_cmp_lt_u32_e64 s[2:3], s2, v0
	v_add_u32_e32 v171, v18, v162
	s_and_saveexec_b64 s[6:7], s[2:3]
	s_xor_b64 s[2:3], exec, s[6:7]
	s_cbranch_execz .LBB1_2
	ds_read_b128 v[34:37], v171
	ds_read_b128 v[38:41], v171 offset:32
	ds_read_b128 v[42:45], v171 offset:80
	ds_read_b128 v[46:49], v171 offset:112
	ds_read_b128 v[172:175], v171 offset:160
	ds_read_b128 v[176:179], v171 offset:192
	ds_read_b128 v[180:183], v171 offset:1600
	ds_read_b128 v[184:187], v171 offset:1632
	ds_read_b128 v[188:191], v171 offset:1680
	s_waitcnt vmcnt(12) lgkmcnt(8)
	v_mfma_f32_32x32x16_f16 v[18:33], v[150:153], v[34:37], v[2:17]
	s_waitcnt lgkmcnt(7)
	v_mfma_f32_32x32x16_f16 v[18:33], v[146:149], v[38:41], v[18:33]
	ds_read_b128 v[34:37], v171 offset:1712
	s_waitcnt lgkmcnt(7)
	v_mfma_f32_32x32x16_f16 v[18:33], v[142:145], v[42:45], v[18:33]
	ds_read_b128 v[38:41], v171 offset:1760
	s_waitcnt lgkmcnt(7)
	v_mfma_f32_32x32x16_f16 v[18:33], v[138:141], v[46:49], v[18:33]
	ds_read_b128 v[42:45], v171 offset:1792
	s_waitcnt lgkmcnt(7)
	v_mfma_f32_32x32x16_f16 v[18:33], v[134:137], v[172:175], v[18:33]
	ds_read_b128 v[46:49], v171 offset:3200
	s_waitcnt lgkmcnt(7)
	v_mfma_f32_32x32x16_f16 v[18:33], v[130:133], v[176:179], v[18:33]
	ds_read_b128 v[172:175], v171 offset:3232
	s_waitcnt lgkmcnt(7)
	v_mfma_f32_32x32x16_f16 v[18:33], v[126:129], v[180:183], v[18:33]
	ds_read_b128 v[176:179], v171 offset:3280
	s_waitcnt lgkmcnt(7)
	v_mfma_f32_32x32x16_f16 v[18:33], v[122:125], v[184:187], v[18:33]
	ds_read_b128 v[180:183], v171 offset:3312
	s_waitcnt lgkmcnt(7)
	v_mfma_f32_32x32x16_f16 v[18:33], v[118:121], v[188:191], v[18:33]
	ds_read_b128 v[184:187], v171 offset:3360
	s_waitcnt lgkmcnt(7)
	v_mfma_f32_32x32x16_f16 v[18:33], v[114:117], v[34:37], v[18:33]
	ds_read_b128 v[188:191], v171 offset:3392
	s_waitcnt lgkmcnt(7)
	v_mfma_f32_32x32x16_f16 v[18:33], v[110:113], v[38:41], v[18:33]
	s_waitcnt lgkmcnt(6)
	v_mfma_f32_32x32x16_f16 v[18:33], v[106:109], v[42:45], v[18:33]
	s_waitcnt lgkmcnt(5)
	v_mfma_f32_32x32x16_f16 v[18:33], v[102:105], v[46:49], v[18:33]
	s_waitcnt lgkmcnt(4)
	v_mfma_f32_32x32x16_f16 v[18:33], v[98:101], v[172:175], v[18:33]
	s_waitcnt lgkmcnt(3)
	v_mfma_f32_32x32x16_f16 v[18:33], v[94:97], v[176:179], v[18:33]
	s_waitcnt lgkmcnt(2)
	v_mfma_f32_32x32x16_f16 v[18:33], v[90:93], v[180:183], v[18:33]
	s_waitcnt lgkmcnt(1)
	v_mfma_f32_32x32x16_f16 v[18:33], v[86:89], v[184:187], v[18:33]
	s_waitcnt lgkmcnt(0)
	v_mfma_f32_32x32x16_f16 v[18:33], v[82:85], v[188:191], v[18:33]
	v_mov_b32_e32 v49, v17
	v_mov_b32_e32 v48, v16
	v_mov_b32_e32 v47, v15
	v_mov_b32_e32 v46, v14
	v_mov_b32_e32 v45, v13
	v_mov_b32_e32 v44, v12
	v_mov_b32_e32 v43, v11
	v_mov_b32_e32 v42, v10
	v_mov_b32_e32 v41, v9
	v_mov_b32_e32 v40, v8
	v_mov_b32_e32 v39, v7
	v_mov_b32_e32 v38, v6
	v_mov_b32_e32 v37, v5
	v_mov_b32_e32 v36, v4
	v_mov_b32_e32 v35, v3
	v_mov_b32_e32 v34, v2
